# one static s_setprio 1 for waves 4-7 at kernel entry (no per-segment flips anywhere)
# baseline (speedup 1.0000x reference)
.LBB0_7:
	s_or_b64 exec, exec, s[4:5]
	s_lshr_b32 s65, s3, 6
	s_cmp_lt_u32 s65, 4
	s_cbranch_scc1 .Lprio_done
	s_setprio 1
.Lprio_done:
	s_cmp_lt_i32 s92, 1
	s_cselect_b64 s[4:5], -1, 0
	s_cmp_gt_i32 s93, 0
	s_cselect_b64 s[6:7], -1, 0
	s_and_b64 s[4:5], s[4:5], s[6:7]
	s_andn2_b64 vcc, exec, s[4:5]
	s_cbranch_vccnz .LBB0_244
	s_mov_b64 s[4:5], s[0:1]
	v_mov_b32_e32 v29, 0
	global_load_dwordx4 v[0:3], v29, s[4:5] offset:16
	global_load_dwordx4 v[24:27], v29, s[4:5]
	global_load_dwordx2 v[152:153], v29, s[4:5] offset:88
	global_load_dwordx4 v[4:7], v29, s[4:5] offset:72
	global_load_dwordx2 v[154:155], v29, s[4:5] offset:168
	global_load_dwordx2 v[30:31], v29, s[4:5] offset:192
	global_load_dwordx4 v[8:11], v29, s[4:5] offset:56
	global_load_dwordx4 v[12:15], v29, s[4:5] offset:40
	global_load_dwordx4 v[16:19], v29, s[4:5] offset:128
	global_load_dwordx4 v[20:23], v29, s[4:5] offset:152
	v_mbcnt_lo_u32_b32 v28, -1, 0
	s_lshl_b32 s28, s64, 3
	s_lshl_b32 s8, s33, 3
	v_mbcnt_hi_u32_b32 v64, -1, v28
	s_add_i32 s36, s28, s65
	s_cmpk_gt_i32 s36, 0x7fff
	v_lshlrev_b32_e32 v60, 3, v64
	s_waitcnt vmcnt(4)
	v_readfirstlane_b32 s6, v30
	v_readfirstlane_b32 s7, v31
	s_cbranch_scc1 .LBB0_11
	v_and_b32_e32 v28, 64, v64
	v_add_u32_e32 v28, 64, v28
	v_xor_b32_e32 v30, 1, v64
	v_cmp_lt_i32_e32 vcc, v30, v28
	s_ashr_i32 s37, s36, 31
	s_lshl_b64 s[4:5], s[36:37], 13
	v_cndmask_b32_e32 v30, v64, v30, vcc
	v_lshlrev_b32_e32 v65, 2, v30
	v_xor_b32_e32 v30, 2, v64
	v_cmp_lt_i32_e32 vcc, v30, v28
	v_lshl_add_u64 v[24:25], v[24:25], 0, s[4:5]
	s_mov_b64 s[4:5], 0x1000
	v_cndmask_b32_e32 v30, v64, v30, vcc
	v_lshlrev_b32_e32 v66, 2, v30
	v_xor_b32_e32 v30, 4, v64
	v_cmp_lt_i32_e32 vcc, v30, v28
	s_ashr_i32 s9, s8, 31
	s_lshl_b64 s[10:11], s[8:9], 13
	v_cndmask_b32_e32 v30, v64, v30, vcc
	v_lshlrev_b32_e32 v67, 2, v30
	v_xor_b32_e32 v30, 8, v64
	v_cmp_lt_i32_e32 vcc, v30, v28
	v_mov_b32_e32 v61, v29
	v_mov_b32_e32 v71, 0x260
	v_cndmask_b32_e32 v30, v64, v30, vcc
	v_lshlrev_b32_e32 v68, 2, v30
	v_xor_b32_e32 v30, 16, v64
	v_cmp_lt_i32_e32 vcc, v30, v28
	s_mov_b32 s14, 0x41fe0000
	s_mov_b32 s15, 0xc2fe0000
	v_cndmask_b32_e32 v30, v64, v30, vcc
	v_lshlrev_b32_e32 v69, 2, v30
	v_xor_b32_e32 v30, 32, v64
	v_cmp_lt_i32_e32 vcc, v30, v28
	s_mov_b32 s16, 0xc0c0400
	s_mov_b32 s17, 0x5040100
	v_cndmask_b32_e32 v28, v64, v30, vcc
	v_lshlrev_b32_e32 v70, 2, v28
	v_lshlrev_b32_e32 v28, 5, v64
	v_lshl_add_u64 v[24:25], v[24:25], 0, v[28:29]
	v_lshl_add_u64 v[24:25], v[24:25], 0, s[4:5]
	s_lshl_b64 s[4:5], s[36:37], 11
	s_add_u32 s4, s6, s4
	s_addc_u32 s5, s7, s5
	v_lshl_add_u64 v[28:29], s[4:5], 0, v[60:61]
	s_mov_b64 s[4:5], 0x42800000
	v_lshl_add_u64 v[62:63], v[28:29], 0, s[4:5]
	s_lshl_b64 s[12:13], s[8:9], 11
	v_mov_b32_e32 v61, 0x358637bd
	s_mov_b32 s9, 0xf800000
	v_mov_b32_e32 v72, 0x42fe0000
	s_mov_b32 s18, s36
